# MoE phases: an XCD's 32 workgroups take 8 row tiles x 4 column tiles per round
# speedup vs baseline: 1.0102x; 1.0102x over previous
; #define LAS __attribute__((address_space(3)))
;     template <class Tp> __device__ __forceinline__ Tp* w(size_t off) const { return (Tp*)(ws + off); }
; __device__ __forceinline__ void expert_offsets(const Frame& F, LAS int* offs, LAS int* cnts, LAS int* rt_exp) {
;     const int* cnt = F.w<int>(WS_CTL) + CW_CNT;
;     __syncthreads();
;     if (F.wave == 0) {
;         const int e = F.lane, cn = cnt[e * CNT_STRIDE], n = (cn + 255) >> 8;
;         int inc = n;
; #pragma unroll
;         for (int o = 1; o < 64; o <<= 1) { const int v = __shfl_up(inc, o); if (e >= o) inc += v; }
;         const int excl = inc - n;
;         cnts[e] = cn; offs[e] = excl * 256; if (e == 63) offs[64] = inc * 256;
;         for (int j = 0; j < n; ++j) rt_exp[excl + j] = e;
;     }
;     __syncthreads();
; }
; __device__ __forceinline__ void ph_moe1(const Frame& F) {
;     LAS int* offs = (LAS int*)(F.lds + LDS_TAB); LAS int* cnts = offs + 128; LAS int* rt_exp = offs + 256;
;     expert_offsets(F, offs, cnts, rt_exp);
;     pg8::GroupedOrder So; So.init(rt_exp, (offs[64] >> 8) * 8, (int)gridDim.x, (int)blockIdx.x);
.LBB0_1008:
	v_writelane_b32 v248, s97, 60
	s_and_b32 s0, s97, 7
	s_lshr_b32 s1, s97, 3
	s_lshr_b32 s74, s0, 1
	s_lshl_b32 s74, s74, 3
	s_lshr_b32 s75, s1, 2
	s_add_i32 s74, s74, s75
	s_lshl_b32 s74, s74, 3
	s_and_b32 s0, s0, 1
	s_lshl_b32 s0, s0, 2
	s_and_b32 s1, s1, 3
	s_or_b32 s0, s0, s1
	s_or_b32 s97, s74, s0
	s_cmp_lt_i32 s80, 8
	s_cselect_b64 s[0:1], -1, 0
	s_and_b64 s[0:1], s[0:1], s[2:3]
	s_andn2_b64 vcc, exec, s[0:1]
	s_cbranch_vccnz .LBB0_1147
	v_readlane_b32 s2, v248, 0
	v_readlane_b32 s3, v248, 1
	s_mov_b64 s[8:9], s[2:3]
	s_mov_b32 s24, s86
	s_load_dword s33, s[2:3], 0xd0
	s_load_dwordx4 s[4:7], s[8:9], 0x90
	s_nop 0
	s_load_dwordx2 s[2:3], s[8:9], 0xb8
	v_mbcnt_lo_u32_b32 v0, -1, 0
	s_mov_b32 s16, 0
	v_mbcnt_hi_u32_b32 v24, -1, v0
	s_cmp_lg_u32 s24, 0
	s_waitcnt vmcnt(0) lgkmcnt(0)
	s_barrier
	s_cbranch_scc1 .LBB0_1026
	v_lshlrev_b32_e32 v0, 8, v24
	v_mov_b32_e32 v1, 0
	v_lshl_add_u64 v[0:1], s[2:3], 0, v[0:1]
	v_add_co_u32_e32 v0, vcc, 0x40000, v0
	v_and_b32_e32 v2, 64, v24
	s_nop 0
	v_addc_co_u32_e32 v1, vcc, 0, v1, vcc
	global_load_dword v1, v[0:1], off
	v_add_u32_e32 v0, -1, v24
	v_cmp_lt_i32_e32 vcc, v0, v2
	v_add_u32_e32 v3, -2, v24
	v_add_u32_e32 v4, -4, v24
	v_cndmask_b32_e32 v0, v0, v24, vcc
	v_lshlrev_b32_e32 v9, 2, v0
	v_cmp_lt_i32_e32 vcc, v3, v2
	v_add_u32_e32 v5, -8, v24
	v_add_u32_e32 v6, -16, v24
	v_cndmask_b32_e32 v3, v3, v24, vcc
	v_cmp_lt_i32_e32 vcc, 0, v24
	v_lshlrev_b32_e32 v3, 2, v3
	v_subrev_u32_e32 v7, 32, v24
	v_lshl_add_u32 v8, v24, 2, 0
	s_waitcnt vmcnt(0)
	v_add_u32_e32 v0, 0xff, v1
	v_ashrrev_i32_e32 v0, 8, v0
	ds_bpermute_b32 v9, v9, v0
	s_waitcnt lgkmcnt(0)
	v_cndmask_b32_e32 v9, 0, v9, vcc
	v_add_u32_e32 v9, v0, v9
	ds_bpermute_b32 v3, v3, v9
	v_cmp_lt_i32_e32 vcc, v4, v2
	s_nop 1
	v_cndmask_b32_e32 v4, v4, v24, vcc
	v_cmp_lt_i32_e32 vcc, 1, v24
	v_lshlrev_b32_e32 v4, 2, v4
	s_waitcnt lgkmcnt(0)
	v_cndmask_b32_e32 v3, 0, v3, vcc
	v_add_u32_e32 v3, v9, v3
	ds_bpermute_b32 v4, v4, v3
	v_cmp_lt_i32_e32 vcc, v5, v2
	s_nop 1
	v_cndmask_b32_e32 v5, v5, v24, vcc
	v_cmp_lt_i32_e32 vcc, 3, v24
	v_lshlrev_b32_e32 v5, 2, v5
	s_waitcnt lgkmcnt(0)
	v_cndmask_b32_e32 v4, 0, v4, vcc
	v_add_u32_e32 v3, v3, v4
	ds_bpermute_b32 v4, v5, v3
	v_cmp_lt_i32_e32 vcc, v6, v2
	s_nop 1
	v_cndmask_b32_e32 v5, v6, v24, vcc
	v_cmp_lt_i32_e32 vcc, 7, v24
	v_lshlrev_b32_e32 v5, 2, v5
	s_waitcnt lgkmcnt(0)
	v_cndmask_b32_e32 v4, 0, v4, vcc
	v_add_u32_e32 v3, v3, v4
	ds_bpermute_b32 v4, v5, v3
	v_cmp_lt_i32_e32 vcc, v7, v2
	v_add_u32_e32 v5, 0x20000, v8
	s_nop 0
	v_cndmask_b32_e32 v2, v7, v24, vcc
	v_cmp_lt_i32_e32 vcc, 15, v24
	v_lshlrev_b32_e32 v2, 2, v2
	s_waitcnt lgkmcnt(0)
	v_cndmask_b32_e32 v4, 0, v4, vcc
	v_add_u32_e32 v3, v3, v4
	ds_bpermute_b32 v2, v2, v3
	v_add_u32_e32 v4, 0x20200, v8
	v_cmp_lt_i32_e32 vcc, 31, v24
	ds_write_b32 v4, v1
	s_waitcnt lgkmcnt(1)
	v_cndmask_b32_e32 v1, 0, v2, vcc
	v_add_u32_e32 v2, v3, v1
	v_sub_u32_e32 v1, v2, v0
	v_lshlrev_b32_e32 v3, 8, v1
	v_cmp_eq_u32_e32 vcc, 63, v24
	ds_write_b32 v5, v3
	s_and_saveexec_b64 s[8:9], vcc
	s_add_i32 s10, 0, 0x20100
	v_lshlrev_b32_e32 v2, 8, v2
	v_mov_b32_e32 v3, s10
	ds_write_b32 v3, v2
	s_or_b64 exec, exec, s[8:9]
	v_cmp_lt_i32_e32 vcc, 0, v0
	s_and_saveexec_b64 s[8:9], vcc
	s_cbranch_execz .LBB0_1025
	v_cmp_ne_u32_e32 vcc, 1, v0
	s_mov_b64 s[12:13], -1
	v_mov_b32_e32 v2, 0
	s_and_saveexec_b64 s[10:11], vcc
	s_cbranch_execz .LBB0_1022
	v_add_u32_e32 v3, -2, v0
	v_lshrrev_b32_e32 v2, 1, v3
	v_add_u32_e32 v2, 1, v2
	v_cmp_lt_u32_e32 vcc, 13, v3
	v_mov_b32_e32 v5, 0
	s_and_saveexec_b64 s[12:13], vcc
	s_cbranch_execz .LBB0_1018
	v_lshl_add_u32 v4, v1, 2, 0
	v_and_b32_e32 v3, -8, v2
	s_mov_b32 s17, 0
	v_add_u32_e32 v4, 0x20400, v4
	s_mov_b64 s[14:15], 0
